# v19 = v16 + expert-up conversion tiles re-indexed so both k-halves of each 128-byte output line are converted in the same workgroup and scan block
# speedup vs baseline: 1.0160x; 1.0160x over previous
; __device__ __forceinline__ ConvTile conv_tile_desc(const unsigned long long* tab, int t) {
;     ...
;     else if (t < CT_C) { const int u = t - CT_B; e = u / 14336; const int v = u % 14336; si = 7; di = 16; N = EXD; K = DM; nb = v % 224; kb = v / 224; mode = 1; }
;     else { const int u = (t < CT_TOTAL ? t : CT_TOTAL - 1) - CT_C; e = u / 7168; const int v = u % 7168; si = 9; di = 17; N = DM; K = EXD; nb = v & 31; kb = v >> 5; }
;     const int n0 = nb * 64;
;     int col0 = n0, nvalid = 64;
;     if (mode) { col0 = (n0 >> 8) * 128 + (n0 & 127); si += (n0 >> 7) & 1; }
;     if (npad) { nvalid = N - n0; if (nvalid <= 0) col0 = 0; }
;     ConvTile c;
;     const size_t KN = (size_t)K * N;
;     c.src = (const float*)tab[si] + (size_t)e * KN + (size_t)(kb * 32) * N + col0;
;     c.dst = (bf16_t*)tab[di] + (size_t)e * (mode ? 2 * KN : KN) + (size_t)n0 * K + kb * 32;
.LBB0_637:
	s_andn2_b64 vcc, exec, s[56:57]
	s_mov_b64 s[62:63], 0
	s_cbranch_vccnz .LBB0_746
	s_add_i32 s56, s72, 0xffff7b00
	s_lshr_b32 s57, s56, 11
	s_mul_hi_u32 s74, s57, 0x24924925
	s_mul_i32 s57, s74, 0x3800
	s_sub_i32 s56, s56, s57
	s_and_b32 s65, s56, 1
	s_lshr_b32 s56, s56, 1
	s_bfe_u32 s57, s56, 0x100005
	s_mulk_i32 s57, 0x2493
	s_lshr_b32 s64, s57, 16
	s_mul_i32 s57, s64, 0xe0
	s_sub_i32 s56, s56, s57
	s_lshl_b32 s64, s64, 1
	s_or_b32 s64, s64, s65
	s_mov_b32 s75, 16
	s_and_b32 s65, s56, 0xffff
	s_mov_b64 s[60:61], 1
	s_mov_b64 s[56:57], 0x800
	s_movk_i32 s96, 0x1c00

; __device__ __forceinline__ ConvTile conv_tile_desc(const unsigned long long* tab, int t) {
;     ...
;     else if (t < CT_C) { const int u = t - CT_B; e = u / 14336; const int v = u % 14336; si = 7; di = 16; N = EXD; K = DM; nb = v % 224; kb = v / 224; mode = 1; }
;     else { const int u = (t < CT_TOTAL ? t : CT_TOTAL - 1) - CT_C; e = u / 7168; const int v = u % 7168; si = 9; di = 17; N = DM; K = EXD; nb = v & 31; kb = v >> 5; }
;     const int n0 = nb * 64;
;     int col0 = n0, nvalid = 64;
;     if (mode) { col0 = (n0 >> 8) * 128 + (n0 & 127); si += (n0 >> 7) & 1; }
;     if (npad) { nvalid = N - n0; if (nvalid <= 0) col0 = 0; }
;     ConvTile c;
;     const size_t KN = (size_t)K * N;
;     c.src = (const float*)tab[si] + (size_t)e * KN + (size_t)(kb * 32) * N + col0;
;     c.dst = (bf16_t*)tab[di] + (size_t)e * (mode ? 2 * KN : KN) + (size_t)n0 * K + kb * 32;
.LBB0_664:
	s_andn2_b64 vcc, exec, s[56:57]
	s_cbranch_vccnz .LBB0_747
	s_add_i32 s56, s72, 0xffff7b00
	s_lshr_b32 s57, s56, 11
	s_mul_hi_u32 s64, s57, 0x24924925
	s_mul_i32 s57, s64, 0x3800
	s_sub_i32 s56, s56, s57
	s_and_b32 s75, s56, 1
	s_lshr_b32 s56, s56, 1
	s_bfe_u32 s57, s56, 0x100005
	s_mulk_i32 s57, 0x2493
	s_lshr_b32 s74, s57, 16
	s_mul_i32 s57, s74, 0xe0
	s_sub_i32 s56, s56, s57
	s_lshl_b32 s74, s74, 1
	s_or_b32 s74, s74, s75
	s_and_b32 s75, s56, 0xffff
	s_mov_b64 s[60:61], 0
	s_mov_b64 s[62:63], 0x800
	s_movk_i32 s56, 0x1c00
	s_mov_b32 s57, 7
	s_mov_b64 s[96:97], 0
